# MoE GEMM phases: expert of a row block found by one LDS read per lane + compare + popcount instead of 16 dependent LDS reads per unit (MoeOrder::next), on top of the BLK0 prefix-sum rewrite
# speedup vs baseline: 1.0105x; 1.0016x over previous
;     __device__ __forceinline__ bool next(int i, Unit& u) const {
;         const int c2 = (G & 7) ? c : (c & 7) * (G >> 3) + (c >> 3);
;         const long Lx = (long)i * G + c2; if (Lx >= nunits) return false;
;         const int j = (int)(Lx / nN), pn = (int)(Lx % nN); int e = 0;
; #pragma unroll
;         for (int k = 1; k < 32; ++k) e += (j >= blk0[k]) ? 1 : 0;
;         u.pm = j; u.pn = pn; u.z = e; u.A = A + (size_t)j * atile; u.B = B + (size_t)e * bexp + (size_t)pn * btile; return true;
.LBB0_3260:
	s_add_i32 s0, s20, 0x20240
	v_mov_b32_e32 v0, s0
	s_add_i32 s1, s20, 0x20420
	ds_read_b32 v2, v0
	s_and_b32 s5, s12, 7
	s_ashr_i32 s6, s24, 3
	v_mov_b32_e32 v0, s1
	s_mul_i32 s5, s5, s6
	ds_read_b64 v[0:1], v0
	s_ashr_i32 s0, s12, 3
	s_and_b32 s4, s24, 7
	s_add_i32 s5, s5, s0
	s_cmp_eq_u32 s4, 0
	s_waitcnt lgkmcnt(1)
	v_lshlrev_b32_e32 v220, 3, v2
	s_cselect_b32 s27, s5, s12
	v_mov_b32_e32 v215, v129
	v_cmp_ge_i32_e32 vcc, s27, v220
	s_waitcnt lgkmcnt(0)
	v_readfirstlane_b32 s17, v1
	v_readfirstlane_b32 s16, v0
	s_nop 0
	v_readfirstlane_b32 s6, v215
	s_cbranch_vccnz .LBB0_3286
	s_add_u32 s8, s2, 0x65200000
	s_addc_u32 s9, s3, 0
	s_add_i32 s28, s20, 0x201c4
	s_ashr_i32 s61, s27, 31
	s_lshr_b32 s0, s61, 29
	s_add_i32 s0, s27, s0
	s_add_i32 s29, s20, 0x201cc
	s_ashr_i32 s96, s0, 3
	s_add_i32 s30, s20, 0x201d4
	s_add_i32 s31, s20, 0x201dc
	s_add_i32 s34, s20, 0x201e4
	s_add_i32 s35, s20, 0x201ec
	s_add_i32 s36, s20, 0x201f4
	s_add_i32 s37, s20, 0x201fc
	s_add_i32 s49, s20, 0x20204
	s_add_i32 s50, s20, 0x2020c
	s_add_i32 s51, s20, 0x20214
	s_add_i32 s56, s20, 0x2021c
	s_add_i32 s57, s20, 0x20224
	s_add_i32 s58, s20, 0x2022c
	s_add_i32 s59, s20, 0x20234
	s_add_i32 s60, s20, 0x2023c
	s_add_i32 s7, s20, 0x20800
	v_mov_b32_e32 v231, v128
	v_mov_b32_e32 v210, v128
	v_cmp_gt_i32_e64 s[0:1], s90, v215
	v_mbcnt_lo_u32_b32 v0, -1, 0
	v_mbcnt_hi_u32_b32 v0, -1, v0
	v_and_b32_e32 v0, 31, v0
	v_max_u32_e32 v0, 1, v0
	v_add_u32_e32 v0, -1, v0
	v_lshl_add_u32 v0, v0, 2, s28
	ds_read_b32 v0, v0
	s_waitcnt lgkmcnt(0)
	v_cmp_ge_i32_e32 vcc, s96, v0
	s_and_b32 vcc_lo, vcc_lo, 0xfffffffe
	s_bcnt1_i32_b32 vcc_lo, vcc_lo
	v_mov_b32_e32 v230, vcc_lo
	s_and_saveexec_b64 s[4:5], s[0:1]
	s_cbranch_execz .LBB0_3263
	v_lshlrev_b32_e32 v0, 2, v230
	v_add_u32_e32 v1, s26, v0
	ds_read_b32 v2, v1
	v_add_u32_e32 v0, s25, v0
	ds_read_b32 v3, v0
	v_lshlrev_b64 v[0:1], 16, v[230:231]
	v_lshl_add_u64 v[0:1], s[8:9], 0, v[0:1]
	s_waitcnt lgkmcnt(1)
	v_sub_u32_e32 v2, s96, v2
	v_lshl_add_u32 v2, v2, 8, v215
	s_waitcnt lgkmcnt(0)
	v_cmp_lt_i32_e32 vcc, v2, v3
	s_nop 1
	v_cndmask_b32_e32 v2, 0, v2, vcc
	v_ashrrev_i32_e32 v3, 31, v2
	v_lshl_add_u64 v[0:1], v[2:3], 2, v[0:1]
	global_load_dword v0, v[0:1], off
	v_lshl_add_u32 v1, v215, 2, s7
	s_waitcnt vmcnt(0)
	ds_write_b32 v1, v0

;     __device__ __forceinline__ bool next(int i, Unit& u) const {
;         const int c2 = (G & 7) ? c : (c & 7) * (G >> 3) + (c >> 3);
;         const long Lx = (long)i * G + c2; if (Lx >= nunits) return false;
;         const int j = (int)(Lx / nN), pn = (int)(Lx % nN); int e = 0;
; #pragma unroll
;         for (int k = 1; k < 32; ++k) e += (j >= blk0[k]) ? 1 : 0;
;         u.pm = j; u.pn = pn; u.z = e; u.A = A + (size_t)j * atile; u.B = B + (size_t)e * bexp + (size_t)pn * btile; return true;
.LBB0_3268:
	s_add_i32 s95, s95, 1
	s_mul_i32 s2, s95, s88
	s_mul_hi_u32 s3, s95, s24
	s_add_i32 s3, s3, s2
	s_mul_i32 s2, s95, s24
	s_add_u32 s4, s2, s27
	s_addc_u32 s5, s3, s61
	v_cmp_ge_i64_e32 vcc, s[4:5], v[220:221]
	v_cmp_lt_i64_e64 s[2:3], s[4:5], v[220:221]
	s_cbranch_vccnz .LBB0_3270
	s_ashr_i32 s6, s5, 31
	s_lshr_b32 s6, s6, 29
	s_add_u32 s6, s4, s6
	s_addc_u32 s7, s5, 0
	s_lshr_b64 s[72:73], s[6:7], 3
	s_and_b32 s6, s6, -8
	s_sub_u32 s74, s4, s6
	v_mov_b32_e32 v227, v128
	s_subb_u32 s75, s5, s7
	s_lshl_b64 s[4:5], s[74:75], 18
	v_mbcnt_lo_u32_b32 v2, -1, 0
	v_mbcnt_hi_u32_b32 v2, -1, v2
	v_and_b32_e32 v2, 31, v2
	v_max_u32_e32 v2, 1, v2
	v_add_u32_e32 v2, -1, v2
	v_lshl_add_u32 v2, v2, 2, s28
	ds_read_b32 v2, v2
	s_waitcnt lgkmcnt(0)
	v_cmp_ge_i32_e32 vcc, s72, v2
	s_and_b32 vcc_lo, vcc_lo, 0xfffffffe
	s_bcnt1_i32_b32 vcc_lo, vcc_lo
	v_mov_b32_e32 v226, vcc_lo
	v_lshlrev_b64 v[2:3], 21, v[226:227]
	v_lshl_add_u64 v[2:3], s[10:11], 0, v[2:3]
	v_lshl_add_u64 v[228:229], v[2:3], 0, s[4:5]

; #define LAS __attribute__((address_space(3)))
; template <class Epi, class Sched, bool ALIGN_EPI = false, bool SP2 = false, bool FP8 = false  ,
;           bool GATHER = false  >
; __device__ __forceinline__ void gemm_phase(LAS unsigned char* lds, const Dims g, const Sched& S, const Epi& E, int tid_in) {
;     ...
;     for (int i = 0; i < 2; ++i) { int R, C; stage_rc(tid * 16 + i * 8192, R, C); const int Rb = Epi::PERM ? ((R & ~31) + perm32(R & 31)) : R;
;         voffA[i] = (unsigned)(R * g.lda + C * 2); voffB[i] = (unsigned)(Rb * g.ldb + C * 2); }
;     static_assert(!GATHER || SP2, "gathered A rows: SP2 schedule only");
;     unsigned vgc[2][2]; bool last_g = false; int nxp_ = 0, gR_ = 0; unsigned gC_ = 0u; (void)last_g; (void)nxp_;
;     if constexpr (GATHER) { int R, C; stage_rc(tid * 16, R, C); gR_ = R; gC_ = (unsigned)(C * 2); }
;     LAS int* const ntok_ = (LAS int*)(lds + GATHER_LIST_OFF);
;     ...
;     const size_t kstep = (size_t)(BK * 2);
;     const size_t hstepA = (size_t)HALF * g.lda, hstepB = (size_t)HALF * g.ldb;
;     const unsigned ldsw = (unsigned)wid * 1024u;
;     const int aoff0 = lds_byte(wr * 64 + fr, fq * 8), aoff1 = aoff0 + 1024;
;     const int boff0 = lds_byte(wc * 32 + fr, fq * 8), boff1 = boff0 + 1024;
;     ...
;     Unit cur, nxt; int ui = 0;
;     if (!S.next(0, cur)) return;
;     f32x4 acc[2][2][4][2];
;     float zq = 0.f; asm volatile("" : "+v"(zq));
; #pragma unroll
;     for (int a = 0; a < 2; ++a)
; #pragma unroll
;         for (int b = 0; b < 2; ++b)
; #pragma unroll
;             for (int m = 0; m < 4; ++m)
; #pragma unroll
;                 for (int n = 0; n < 2; ++n) acc[a][b][m][n] = (f32x4){zq, zq, zq, zq};
;     bf16x8 At[4][2], B0[2][2], B1[2][2];
;     const char* cA = cur.A; const char* cB = cur.B;
;     if constexpr (SP2) {
;         if constexpr (GATHER) { PG8_GLIST(cur, 0); PG8_WAIT_L(0); PG8_BAR; PG8_GOFF(0, vgc); }
;     __device__ __forceinline__ bool next(int i, Unit& u) const {
;         const int c2 = (G & 7) ? c : (c & 7) * (G >> 3) + (c >> 3);
;         const long Lx = (long)i * G + c2; if (Lx >= nunits) return false;
;         const int j = (int)(Lx / nN), pn = (int)(Lx % nN); int e = 0;
; #pragma unroll
;         for (int k = 1; k < 32; ++k) e += (j >= blk0[k]) ? 1 : 0;
;         u.pm = j; u.pn = pn; u.z = e; u.A = A + (size_t)j * atile; u.B = B + (size_t)e * bexp + (size_t)pn * btile; return true;
.LBB0_3415:
	s_or_b64 exec, exec, s[0:1]
	s_add_i32 s0, s14, 0x20240
	v_mov_b32_e32 v0, s0
	s_add_i32 s1, s14, 0x20430
	s_waitcnt lgkmcnt(0)
	s_barrier
	ds_read_b32 v2, v0
	s_and_b32 s3, s4, 7
	s_ashr_i32 s5, s26, 3
	v_mov_b32_e32 v0, s1
	s_mul_i32 s3, s3, s5
	ds_read_b64 v[0:1], v0
	s_ashr_i32 s0, s4, 3
	s_and_b32 s2, s26, 7
	s_add_i32 s3, s3, s0
	s_cmp_eq_u32 s2, 0
	s_waitcnt lgkmcnt(1)
	v_lshlrev_b32_e32 v146, 2, v2
	s_cselect_b32 s27, s3, s4
	v_mov_b32_e32 v12, v129
	v_cmp_ge_i32_e32 vcc, s27, v146
	s_waitcnt lgkmcnt(0)
	v_readfirstlane_b32 s7, v1
	v_readfirstlane_b32 s6, v0
	s_nop 0
	v_readfirstlane_b32 s0, v12
	s_cbranch_vccnz .LBB0_3431
	v_lshlrev_b32_e32 v0, 4, v12
	v_add_u32_e32 v1, 0x2000, v0
	v_ashrrev_i32_e32 v2, 31, v1
	v_lshrrev_b32_e32 v2, 22, v2
	v_add_u32_e32 v2, v1, v2
	v_ashrrev_i32_e32 v6, 10, v2
	v_mul_i32_i24_e32 v2, 0x400, v6
	v_sub_u32_e32 v1, v1, v2
	v_lshrrev_b32_e32 v2, 4, v1
	v_bitop3_b32 v1, v2, v1, 32 bitop3:0x6c
	v_ashrrev_i32_e32 v2, 31, v1
	v_lshrrev_b32_e32 v2, 26, v2
	v_add_u32_e32 v2, v1, v2
	v_lshlrev_b32_e32 v3, 3, v6
	v_ashrrev_i32_e32 v7, 6, v2
	v_and_b32_e32 v3, -16, v3
	v_add_u32_e32 v3, v7, v3
	v_and_b32_e32 v4, 3, v7
	s_mov_b32 s4, 0x3fffe0
	v_lshrrev_b32_e32 v5, 2, v3
	v_lshlrev_b32_e32 v8, 1, v3
	v_and_b32_e32 v2, 0xc0, v2
	v_and_or_b32 v4, v3, s4, v4
	v_and_b32_e32 v5, 4, v5
	v_and_b32_e32 v8, 24, v8
	v_sub_u32_e32 v1, v1, v2
	v_or3_b32 v4, v4, v5, v8
	v_lshlrev_b32_e32 v5, 5, v6
	v_ashrrev_i16_sdwa v1, v248, sext(v1) dst_sel:DWORD dst_unused:UNUSED_PAD src0_sel:DWORD src1_sel:BYTE_0
	v_and_b32_e32 v5, 32, v5
	v_bfe_i32 v8, v1, 0, 16
	v_add_lshl_u32 v1, v5, v8, 1
	v_lshl_add_u32 v148, v4, 10, v1
	v_lshl_add_u32 v150, v3, 10, v1
	v_bfe_i32 v1, v12, 27, 1
	v_lshrrev_b32_e32 v1, 22, v1
	v_add_u32_e32 v1, v0, v1
	v_and_b32_e32 v1, 0xfffffc00, v1
	v_sub_u32_e32 v0, v0, v1
	v_lshrrev_b32_e32 v1, 4, v0
	v_ashrrev_i32_e32 v2, 31, v12
	v_bitop3_b32 v0, v1, v0, 32 bitop3:0x6c
	v_lshrrev_b32_e32 v2, 26, v2
	v_ashrrev_i32_e32 v1, 31, v0
	v_add_u32_e32 v2, v12, v2
	v_lshrrev_b32_e32 v1, 26, v1
	v_ashrrev_i32_e32 v10, 6, v2
	s_ashr_i32 s8, s0, 6
	v_add_u32_e32 v1, v0, v1
	v_lshlrev_b32_e32 v2, 3, v10
	s_lshl_b32 s22, s62, 15
	s_ashr_i32 s9, s0, 8
	s_lshl_b32 s1, s8, 10
	v_ashrrev_i32_e32 v9, 6, v1
	v_and_b32_e32 v2, -16, v2
	s_add_u32 s28, s10, 0x6e640000
	v_add_u32_e32 v2, v9, v2
	s_addc_u32 s29, s11, 0
	s_lshl_b64 s[2:3], s[22:23], 10
	v_and_b32_e32 v3, 3, v9
	v_lshrrev_b32_e32 v4, 2, v2
	v_lshlrev_b32_e32 v5, 1, v2
	v_and_b32_e32 v1, 0xc0, v1
	s_add_u32 s2, s10, s2
	v_and_or_b32 v3, v2, s4, v3
	v_and_b32_e32 v4, 4, v4
	v_and_b32_e32 v5, 24, v5
	v_sub_u32_e32 v0, v0, v1
	s_addc_u32 s3, s11, s3
	v_or3_b32 v3, v3, v4, v5
	v_lshlrev_b32_e32 v4, 5, v10
	v_ashrrev_i16_sdwa v0, v248, sext(v0) dst_sel:DWORD dst_unused:UNUSED_PAD src0_sel:DWORD src1_sel:BYTE_0
	s_add_u32 s2, s2, 0x26700000
	v_and_b32_e32 v4, 32, v4
	v_bfe_i32 v11, v0, 0, 16
	s_addc_u32 s3, s3, 0
	s_add_i32 s30, s14, 0x201c4
	v_add_lshl_u32 v0, v4, v11, 1
	v_lshl_add_u32 v152, v3, 10, v0
	v_lshl_add_u32 v154, v2, 10, v0
	s_ashr_i32 s67, s27, 31
	s_lshr_b32 s4, s67, 30
	s_add_i32 s4, s27, s4
	s_add_i32 s31, s14, 0x201cc
	s_ashr_i32 s18, s4, 2
	s_add_i32 s34, s14, 0x201d4
	s_add_i32 s35, s14, 0x201dc
	s_add_i32 s36, s14, 0x201e4
	s_add_i32 s37, s14, 0x201ec
	s_add_i32 s49, s14, 0x201f4
	s_add_i32 s50, s14, 0x201fc
	s_add_i32 s51, s14, 0x20204
	s_add_i32 s56, s14, 0x2020c
	s_add_i32 s57, s14, 0x20214
	s_add_i32 s58, s14, 0x2021c
	s_add_i32 s59, s14, 0x20224
	s_add_i32 s60, s14, 0x2022c
	s_add_i32 s61, s14, 0x20234
	s_mov_b32 s46, s62
	s_add_i32 s62, s14, 0x2023c
	s_and_b32 s4, s4, -4
	s_ashr_i32 s19, s18, 31
	s_sub_i32 s68, s27, s4
	s_add_i32 s63, s14, 0x10000
	s_add_i32 s66, s14, 0x14000
	s_ashr_i32 s69, s68, 31
	s_lshl_b64 s[4:5], s[18:19], 18
	v_mov_b32_e32 v117, v128
	s_add_u32 s20, s28, s4
	s_addc_u32 s21, s29, s5
	s_lshl_b64 s[4:5], s[68:69], 18
	s_add_i32 s19, s63, s1
	v_mov_b32_e32 v164, v128
	s_mov_b32 m0, s19
	s_add_i32 s69, s19, 0x2000
	s_add_i32 s72, s66, s1
	s_add_i32 s73, s72, 0x2000
	s_add_i32 s74, s14, s1
	s_add_i32 s75, s74, 0x2000
	v_mov_b32_e32 v155, v128
	v_mov_b32_e32 v151, v128
	v_lshl_add_u64 v[4:5], s[20:21], 0, v[150:151]
	v_mbcnt_lo_u32_b32 v0, -1, 0
	v_mbcnt_hi_u32_b32 v0, -1, v0
	v_and_b32_e32 v0, 31, v0
	v_max_u32_e32 v0, 1, v0
	v_add_u32_e32 v0, -1, v0
	v_lshl_add_u32 v0, v0, 2, s30
	ds_read_b32 v0, v0
	s_waitcnt lgkmcnt(0)
	v_cmp_ge_i32_e32 vcc, s18, v0
	s_and_b32 vcc_lo, vcc_lo, 0xfffffffe
	s_bcnt1_i32_b32 vcc_lo, vcc_lo
	v_mov_b32_e32 v116, vcc_lo
	v_lshlrev_b64 v[0:1], 20, v[116:117]
	v_lshl_add_u64 v[0:1], s[2:3], 0, v[0:1]
	v_lshl_add_u64 v[0:1], v[0:1], 0, s[4:5]
	v_lshl_add_u64 v[2:3], v[0:1], 0, s[38:39]
	v_readfirstlane_b32 s4, v0
	v_readfirstlane_b32 s5, v1
	s_nop 4
	global_load_lds_dwordx4 v152, s[4:5]
	s_mov_b32 m0, s69
	s_nop 0
	global_load_lds_dwordx4 v148, s[4:5]
	s_mov_b32 m0, s72
	v_readfirstlane_b32 s4, v2
	v_readfirstlane_b32 s5, v3
	v_lshl_add_u64 v[2:3], s[20:21], 0, v[154:155]
	s_nop 3
	global_load_lds_dwordx4 v152, s[4:5]
	s_mov_b32 m0, s73
	s_nop 0
	global_load_lds_dwordx4 v148, s[4:5]
	s_mov_b32 m0, s74
	s_add_u32 s4, s20, 0x20000
	global_load_lds_dwordx4 v154, s[20:21]
	s_mov_b32 m0, s75
	s_addc_u32 s5, s21, 0
	s_add_i32 s76, s74, 0x4000
	global_load_lds_dwordx4 v150, s[20:21]
	s_mov_b32 m0, s76
	s_add_i32 s77, s74, 0x6000
	global_load_lds_dwordx4 v154, s[4:5]
	s_mov_b32 m0, s77
	s_cmp_eq_u32 s9, 1
	global_load_lds_dwordx4 v150, s[4:5]
	s_cselect_b64 s[4:5], -1, 0
	s_cmp_lg_u32 s9, 1
	s_cbranch_scc1 .LBB0_3418
	s_barrier

;     __device__ __forceinline__ bool next(int i, Unit& u) const {
;         const int c2 = (G & 7) ? c : (c & 7) * (G >> 3) + (c >> 3);
;         const long Lx = (long)i * G + c2; if (Lx >= nunits) return false;
;         const int j = (int)(Lx / nN), pn = (int)(Lx % nN); int e = 0;
; #pragma unroll
;         for (int k = 1; k < 32; ++k) e += (j >= blk0[k]) ? 1 : 0;
;         u.pm = j; u.pn = pn; u.z = e; u.A = A + (size_t)j * atile; u.B = B + (size_t)e * bexp + (size_t)pn * btile; return true;
.LBB0_3421:
	s_add_i32 s90, s90, 1
	s_mul_i32 s0, s90, s83
	s_mul_hi_u32 s1, s90, s26
	s_add_i32 s1, s1, s0
	s_mul_i32 s0, s90, s26
	s_add_u32 s24, s0, s27
	s_addc_u32 s25, s1, s67
	v_cmp_ge_i64_e32 vcc, s[24:25], v[146:147]
	v_cmp_lt_i64_e64 s[0:1], s[24:25], v[146:147]
	s_cbranch_vccnz .LBB0_3423
	s_ashr_i32 s14, s25, 31
	s_lshr_b32 s14, s14, 30
	s_add_u32 s16, s24, s14
	s_addc_u32 s17, s25, 0
	s_lshr_b64 s[14:15], s[16:17], 2
	s_and_b32 s15, s16, -4
	s_sub_u32 s16, s24, s15
	s_subb_u32 s17, s25, s17
	s_mov_b32 s24, s23
	s_mov_b32 s25, s14
	s_ashr_i64 s[24:25], s[24:25], 14
	v_mov_b32_e32 v161, v128
	s_add_u32 s70, s28, s24
	s_addc_u32 s71, s29, s25
	s_lshl_b64 s[24:25], s[16:17], 18
	v_mbcnt_lo_u32_b32 v2, -1, 0
	v_mbcnt_hi_u32_b32 v2, -1, v2
	v_and_b32_e32 v2, 31, v2
	v_max_u32_e32 v2, 1, v2
	v_add_u32_e32 v2, -1, v2
	v_lshl_add_u32 v2, v2, 2, s30
	ds_read_b32 v2, v2
	s_waitcnt lgkmcnt(0)
	v_cmp_ge_i32_e32 vcc, s14, v2
	s_and_b32 vcc_lo, vcc_lo, 0xfffffffe
	s_bcnt1_i32_b32 vcc_lo, vcc_lo
	v_mov_b32_e32 v160, vcc_lo
	v_lshlrev_b64 v[2:3], 20, v[160:161]
	v_lshl_add_u64 v[2:3], s[2:3], 0, v[2:3]
	v_lshl_add_u64 v[162:163], v[2:3], 0, s[24:25]
